# v9_p2merge
# speedup vs baseline: 1.0538x; 1.0131x over previous
.LBB1_114:
	s_sub_i32 s54, 3, s59
	s_cmp_ge_u32 s86, s54
	s_waitcnt lgkmcnt(0)
	s_barrier
	s_cbranch_scc1 .LBB1_116
	s_add_i32 s54, s59, s92
	s_lshl_b32 s54, s54, 4
	v_or_b32_e32 v66, s54, v131
	s_lshl_b32 s55, s96, 2
	v_mul_lo_u32 v66, v66, s95
	v_add3_u32 v70, v159, s55, v66
	ds_read2_b32 v[66:67], v70 offset1:4
	v_mul_lo_u32 v68, v164, s95
	v_add3_u32 v71, s55, v68, v130
	ds_read2_b32 v[68:69], v71 offset1:4
	ds_read2_b32 v[72:73], v71 offset0:8 offset1:12
	ds_read2_b32 v[70:71], v70 offset0:8 offset1:12
	v_or_b32_e32 v166, s54, v130
	v_mul_lo_u32 v166, v166, s95
	v_add3_u32 v166, v163, v166, s85
	s_waitcnt lgkmcnt(2)
	v_mfma_f32_16x16x4_f32 a[0:3], v66, v68, 0
	v_mfma_f32_16x16x4_f32 a[0:3], v67, v69, a[0:3]
	s_waitcnt lgkmcnt(0)
	v_mfma_f32_16x16x4_f32 a[0:3], v70, v72, a[0:3]
	v_mfma_f32_16x16x4_f32 a[0:3], v71, v73, a[0:3]
	s_nop 9
	ds_write_b32 v166, a0
	ds_write_b32 v166, a1 offset:272
	ds_write_b32 v166, a2 offset:544
	ds_write_b32 v166, a3 offset:816

.LBB1_235:
	s_sub_i32 s52, 3, s59
	s_cmp_ge_u32 s86, s52
	s_waitcnt lgkmcnt(0)
	s_barrier
	s_cbranch_scc1 .LBB1_237
	s_add_i32 s52, s59, s92
	s_lshl_b32 s52, s52, 4
	v_or_b32_e32 v2, s52, v131
	s_lshl_b32 s53, s97, 2
	v_mul_lo_u32 v2, v2, s57
	v_add3_u32 v6, v10, s53, v2
	ds_read2_b32 v[2:3], v6 offset1:4
	v_mul_lo_u32 v4, v14, s57
	v_add3_u32 v7, s53, v4, v130
	ds_read2_b32 v[4:5], v7 offset1:4
	ds_read2_b32 v[8:9], v7 offset0:8 offset1:12
	ds_read2_b32 v[6:7], v6 offset0:8 offset1:12
	v_or_b32_e32 v16, s52, v130
	v_mul_lo_u32 v16, v16, s57
	v_add3_u32 v16, v13, v16, s95
	s_waitcnt lgkmcnt(2)
	v_mfma_f32_16x16x4_f32 a[0:3], v2, v4, 0
	v_mfma_f32_16x16x4_f32 a[0:3], v3, v5, a[0:3]
	s_waitcnt lgkmcnt(0)
	v_mfma_f32_16x16x4_f32 a[0:3], v6, v8, a[0:3]
	v_mfma_f32_16x16x4_f32 a[0:3], v7, v9, a[0:3]
	s_nop 9
	ds_write_b32 v16, a0
	ds_write_b32 v16, a1 offset:272
	ds_write_b32 v16, a2 offset:544
	ds_write_b32 v16, a3 offset:816

.LBB1_305:
	s_sub_i32 s52, 3, s79
	s_cmp_ge_u32 s86, s52
	s_waitcnt lgkmcnt(0)
	s_barrier
	s_cbranch_scc1 .LBB1_307
	s_add_i32 s52, s79, s76
	s_lshl_b32 s52, s52, 4
	v_or_b32_e32 v2, s52, v19
	s_lshl_b32 s53, s80, 2
	v_mul_lo_u32 v2, v2, s78
	v_add3_u32 v6, v1, s53, v2
	ds_read2_b32 v[2:3], v6 offset1:4
	v_mul_lo_u32 v4, v42, s78
	v_add3_u32 v7, s53, v4, v18
	ds_read2_b32 v[4:5], v7 offset1:4
	ds_read2_b32 v[8:9], v7 offset0:8 offset1:12
	ds_read2_b32 v[6:7], v6 offset0:8 offset1:12
	v_or_b32_e32 v53, s52, v18
	v_mul_lo_u32 v53, v53, s78
	v_add3_u32 v53, v41, v53, s69
	s_waitcnt lgkmcnt(2)
	v_mfma_f32_16x16x4_f32 a[0:3], v2, v4, 0
	v_mfma_f32_16x16x4_f32 a[0:3], v3, v5, a[0:3]
	s_waitcnt lgkmcnt(0)
	v_mfma_f32_16x16x4_f32 a[0:3], v6, v8, a[0:3]
	v_mfma_f32_16x16x4_f32 a[0:3], v7, v9, a[0:3]
	s_nop 9
	ds_write_b32 v53, a0
	ds_write_b32 v53, a1 offset:272
	ds_write_b32 v53, a2 offset:544
	ds_write_b32 v53, a3 offset:816

.LBB1_346:
	s_sub_i32 s52, 3, s74
	s_cmp_ge_u32 s86, s52
	s_waitcnt lgkmcnt(0)
	s_barrier
	s_cbranch_scc1 .LBB1_348
	s_add_i32 s52, s74, s76
	s_lshl_b32 s52, s52, 4
	v_or_b32_e32 v0, s52, v19
	s_lshl_b32 s53, s75, 2
	v_mul_lo_u32 v0, v0, s64
	v_add3_u32 v4, v8, s53, v0
	ds_read2_b32 v[0:1], v4 offset1:4
	v_mul_lo_u32 v2, v34, s64
	v_add3_u32 v5, s53, v2, v18
	ds_read2_b32 v[2:3], v5 offset1:4
	ds_read2_b32 v[6:7], v5 offset0:8 offset1:12
	ds_read2_b32 v[4:5], v4 offset0:8 offset1:12
	v_or_b32_e32 v36, s52, v18
	v_mul_lo_u32 v36, v36, s64
	v_add3_u32 v36, v14, v36, s72
	s_waitcnt lgkmcnt(2)
	v_mfma_f32_16x16x4_f32 a[0:3], v0, v2, 0
	v_mfma_f32_16x16x4_f32 a[0:3], v1, v3, a[0:3]
	s_waitcnt lgkmcnt(0)
	v_mfma_f32_16x16x4_f32 a[0:3], v4, v6, a[0:3]
	v_mfma_f32_16x16x4_f32 a[0:3], v5, v7, a[0:3]
	s_nop 9
	ds_write_b32 v36, a0
	ds_write_b32 v36, a1 offset:272
	ds_write_b32 v36, a2 offset:544
	ds_write_b32 v36, a3 offset:816
